# v76 + attention KV-tile loops: Q.K^T fragment LDS reads issued right after the loop-head barrier, before the next tile's LDS-DMA issue block (loop-edge reordering, guide section 7.11 family)
# speedup vs baseline: 1.0107x; 1.0078x over previous
.LBB0_3619:
	s_waitcnt vmcnt(0)
	s_lshl_b32 s98, s2, 15
	s_cmp_lg_u32 s3, 0
	s_waitcnt vmcnt(0) lgkmcnt(0)
	s_barrier
	v_add3_u32 v0, s98, v123, v124
	ds_read_b128 v[34:37], v0
	ds_read_b128 v[50:53], v0 offset:512
	ds_read_b128 v[128:131], v0 offset:2048
	ds_read_b128 v[132:135], v0 offset:2560
	s_cbranch_scc0 .LBB0_3632
	s_lshl_b32 s0, s2, 15
	s_ff1_i32_b32 s47, s3
	s_xor_b32 s6, s0, 0x8000
	s_lshl_b32 s92, s47, 14
	s_add_i32 s6, s46, s6
	v_lshl_add_u64 v[198:199], v[84:85], 0, s[92:93]
	s_mov_b32 m0, s6
	s_nop 0
	global_load_lds_dwordx4 v[198:199], off
	v_lshl_add_u64 v[198:199], v[82:83], 0, s[92:93]
	s_add_i32 m0, s6, 0x4000
	s_add_i32 s6, s3, -1
	global_load_lds_dwordx4 v[198:199], off
	s_and_b32 s3, s6, s3
	s_cbranch_execnz .LBB0_3622

.LBB0_3622:
	s_add_i32 s0, s0, 0
	s_lshl_b32 s6, s8, 6
	v_readfirstlane_b32 s7, v119
	s_or_b32 s8, s6, 63
	s_cmp_le_i32 s8, s7
	s_cselect_b64 s[8:9], -1, 0
	s_waitcnt lgkmcnt(0)
	v_mfma_f32_32x32x16_bf16 v[34:49], v[34:37], v[66:69], 0
	s_addk_i32 s7, 0xff9f
	s_cmp_gt_i32 s6, s7
	s_cselect_b64 s[10:11], -1, 0
	s_and_b64 s[8:9], s[8:9], s[10:11]
	s_and_b64 vcc, exec, s[8:9]
	v_mfma_f32_32x32x16_bf16 v[50:65], v[50:53], v[66:69], 0
	ds_read_b128 v[136:139], v0 offset:4096
	ds_read_b128 v[140:143], v0 offset:4608
	v_mfma_f32_32x32x16_bf16 v[34:49], v[128:131], v[70:73], v[34:49]
	v_mfma_f32_32x32x16_bf16 v[50:65], v[132:135], v[70:73], v[50:65]
	ds_read_b128 v[128:131], v0 offset:6144
	ds_read_b128 v[132:135], v0 offset:6656
	s_waitcnt lgkmcnt(0)
	v_mfma_f32_32x32x16_bf16 v[34:49], v[136:139], v[74:77], v[34:49]
	v_mfma_f32_32x32x16_bf16 v[50:65], v[140:143], v[74:77], v[50:65]
	v_mfma_f32_32x32x16_bf16 v[34:49], v[128:131], v[78:81], v[34:49]
	v_mfma_f32_32x32x16_bf16 v[50:65], v[132:135], v[78:81], v[50:65]
	s_cbranch_vccnz .LBB0_3626
	v_or_b32_e32 v0, s6, v127
	v_sub_u32_e32 v0, v119, v0
	v_subrev_u32_e32 v128, 32, v0
	v_cmp_gt_u32_e64 s[6:7], s57, v128
	v_add_u32_e32 v128, -1, v0
	v_cmp_gt_u32_e32 vcc, s57, v0
	s_nop 4
	v_cndmask_b32_e64 v50, v240, v50, s[6:7]
	v_cmp_gt_u32_e64 s[6:7], s57, v128
	v_subrev_u32_e32 v128, 33, v0
	v_cmp_gt_u32_e64 s[8:9], s57, v128
	v_add_u32_e32 v128, -2, v0
	s_nop 0
	v_cndmask_b32_e64 v51, v240, v51, s[8:9]
	v_cmp_gt_u32_e64 s[8:9], s57, v128
	v_subrev_u32_e32 v128, 34, v0
	v_cmp_gt_u32_e64 s[10:11], s57, v128
	v_add_u32_e32 v128, -3, v0
	s_nop 0
	v_cndmask_b32_e64 v52, v240, v52, s[10:11]
	v_cmp_gt_u32_e64 s[10:11], s57, v128
	v_subrev_u32_e32 v128, 35, v0
	v_cmp_gt_u32_e64 s[12:13], s57, v128
	v_add_u32_e32 v128, -8, v0
	s_nop 0
	v_cndmask_b32_e64 v53, v240, v53, s[12:13]
	v_cmp_gt_u32_e64 s[12:13], s57, v128
	v_subrev_u32_e32 v128, 40, v0
	v_cmp_gt_u32_e64 s[14:15], s57, v128
	v_add_u32_e32 v128, -9, v0
	s_nop 0
	v_cndmask_b32_e64 v54, v240, v54, s[14:15]
	v_cmp_gt_u32_e64 s[14:15], s57, v128
	v_subrev_u32_e32 v128, 41, v0
	v_cmp_gt_u32_e64 s[16:17], s57, v128
	v_add_u32_e32 v128, -10, v0
	s_nop 0
	v_cndmask_b32_e64 v55, v240, v55, s[16:17]
	v_cmp_gt_u32_e64 s[16:17], s57, v128
	v_subrev_u32_e32 v128, 42, v0
	v_cmp_gt_u32_e64 s[18:19], s57, v128
	v_add_u32_e32 v128, -11, v0
	s_nop 0
	v_cndmask_b32_e64 v56, v240, v56, s[18:19]
	v_cmp_gt_u32_e64 s[18:19], s57, v128
	v_subrev_u32_e32 v128, 43, v0
	v_cmp_gt_u32_e64 s[20:21], s57, v128
	v_add_u32_e32 v128, -16, v0
	s_nop 0
	v_cndmask_b32_e64 v57, v240, v57, s[20:21]
	v_cmp_gt_u32_e64 s[20:21], s57, v128
	v_subrev_u32_e32 v128, 48, v0
	v_cmp_gt_u32_e64 s[22:23], s57, v128
	v_subrev_u32_e32 v128, 17, v0
	s_nop 0
	v_cndmask_b32_e64 v58, v240, v58, s[22:23]
	v_cmp_gt_u32_e64 s[22:23], s57, v128
	v_subrev_u32_e32 v128, 49, v0
	v_cmp_gt_u32_e64 s[24:25], s57, v128
	v_subrev_u32_e32 v128, 18, v0
	s_nop 0
	v_cndmask_b32_e64 v59, v240, v59, s[24:25]
	v_cmp_gt_u32_e64 s[24:25], s57, v128
	v_subrev_u32_e32 v128, 50, v0
	v_cmp_gt_u32_e64 s[26:27], s57, v128
	v_subrev_u32_e32 v128, 19, v0
	s_nop 0
	v_cndmask_b32_e64 v60, v240, v60, s[26:27]
	v_cmp_gt_u32_e64 s[26:27], s57, v128
	v_subrev_u32_e32 v128, 51, v0
	v_cmp_gt_u32_e64 s[28:29], s57, v128
	v_subrev_u32_e32 v128, 24, v0
	s_nop 0
	v_cndmask_b32_e64 v61, v240, v61, s[28:29]
	v_cmp_gt_u32_e64 s[28:29], s57, v128
	v_subrev_u32_e32 v128, 56, v0
	v_cmp_gt_u32_e64 s[30:31], s57, v128
	v_subrev_u32_e32 v128, 25, v0
	s_nop 0
	v_cndmask_b32_e64 v62, v240, v62, s[30:31]
	v_cmp_gt_u32_e64 s[30:31], s57, v128
	v_subrev_u32_e32 v128, 57, v0
	v_cmp_gt_u32_e64 s[34:35], s57, v128
	v_subrev_u32_e32 v128, 26, v0
	s_nop 0
	v_cndmask_b32_e64 v63, v240, v63, s[34:35]
	v_cmp_gt_u32_e64 s[34:35], s57, v128
	v_subrev_u32_e32 v128, 58, v0
	v_cmp_gt_u32_e64 s[36:37], s57, v128
	v_subrev_u32_e32 v128, 27, v0
	v_subrev_u32_e32 v0, 59, v0
	v_cndmask_b32_e64 v64, v240, v64, s[36:37]
	v_cmp_gt_u32_e64 s[36:37], s57, v128
	v_cmp_lt_u32_e64 s[38:39], s60, v0
	s_and_saveexec_b64 s[44:45], s[38:39]
	v_mov_b32_e32 v65, s61
	s_or_b64 exec, exec, s[44:45]
	v_cndmask_b32_e32 v34, v240, v34, vcc
	v_cndmask_b32_e64 v35, v240, v35, s[6:7]
	v_cndmask_b32_e64 v36, v240, v36, s[8:9]
	v_cndmask_b32_e64 v37, v240, v37, s[10:11]
	v_cndmask_b32_e64 v38, v240, v38, s[12:13]
	v_cndmask_b32_e64 v39, v240, v39, s[14:15]
	v_cndmask_b32_e64 v40, v240, v40, s[16:17]
	v_cndmask_b32_e64 v41, v240, v41, s[18:19]
	v_cndmask_b32_e64 v42, v240, v42, s[20:21]
	v_cndmask_b32_e64 v43, v240, v43, s[22:23]
	v_cndmask_b32_e64 v44, v240, v44, s[24:25]
	v_cndmask_b32_e64 v45, v240, v45, s[26:27]
	v_cndmask_b32_e64 v46, v240, v46, s[28:29]
	v_cndmask_b32_e64 v47, v240, v47, s[30:31]
	v_cndmask_b32_e64 v48, v240, v48, s[34:35]
	v_cndmask_b32_e64 v49, v240, v49, s[36:37]

.LBB0_3637:
	s_waitcnt vmcnt(0)
	s_lshl_b32 s98, s53, 15
	s_add_i32 s98, s98, s51
	s_cmp_lg_u32 s52, 0
	s_waitcnt lgkmcnt(0)
	s_barrier
	v_add3_u32 v14, s98, v136, v137
	ds_read_b128 v[2:5], v14
	ds_read_b128 v[6:9], v14 offset:512
	ds_read_b128 v[10:13], v14 offset:2048
	ds_read_b128 v[142:145], v14 offset:2560
	s_cbranch_scc0 .LBB0_3650
	s_lshl_b32 s7, s53, 15
	s_xor_b32 s4, s7, 0x8000
	s_ff1_i32_b32 s54, s52
	s_add_i32 s4, s4, 0
	s_lshl_b32 s92, s54, 16
	s_add_i32 s5, s4, s0
	v_lshl_add_u64 v[198:199], v[130:131], 0, s[92:93]
	s_mov_b32 m0, s5
	s_add_i32 s4, s4, s50
	global_load_lds_dwordx4 v[198:199], off
	v_lshl_add_u64 v[198:199], v[198:199], 0, s[96:97]
	s_add_i32 m0, s5, 0x2000
	s_nop 0
	global_load_lds_dwordx4 v[198:199], off
	v_lshl_add_u64 v[198:199], v[132:133], 0, s[92:93]
	v_lshl_add_u64 v[200:201], s[42:43], 1, v[198:199]
	s_add_i32 m0, s5, 0x4000
	v_lshl_add_u64 v[198:199], s[44:45], 1, v[198:199]
	global_load_lds_dwordx4 v[200:201], off
	s_add_i32 m0, s4, 0x4000
	s_add_i32 s4, s52, -1
	global_load_lds_dwordx4 v[198:199], off
	s_and_b32 s52, s4, s52
	s_cbranch_execnz .LBB0_3640

.LBB0_3640:
	s_add_i32 s55, s7, 0
	s_add_i32 s4, s55, s51
	s_lshl_b32 s4, s6, 6
	v_readfirstlane_b32 s5, v134
	s_or_b32 s6, s4, 63
	s_cmp_le_i32 s6, s5
	s_cselect_b64 s[6:7], -1, 0
	s_waitcnt lgkmcnt(0)
	v_mfma_f32_32x32x16_bf16 v[96:111], v[2:5], v[112:115], 0
	s_add_i32 s5, s5, 0xf000001f
	s_cmp_gt_i32 s4, s5
	s_cselect_b64 s[8:9], -1, 0
	s_and_b64 s[6:7], s[6:7], s[8:9]
	s_and_b64 vcc, exec, s[6:7]
	v_mfma_f32_32x32x16_bf16 v[80:95], v[6:9], v[112:115], 0
	ds_read_b128 v[2:5], v14 offset:4096
	ds_read_b128 v[6:9], v14 offset:4608
	v_mfma_f32_32x32x16_bf16 v[96:111], v[10:13], v[116:119], v[96:111]
	v_mfma_f32_32x32x16_bf16 v[80:95], v[142:145], v[116:119], v[80:95]
	ds_read_b128 v[10:13], v14 offset:6144
	ds_read_b128 v[142:145], v14 offset:6656
	s_waitcnt lgkmcnt(0)
	v_mfma_f32_32x32x16_bf16 v[96:111], v[2:5], v[120:123], v[96:111]
	v_mfma_f32_32x32x16_bf16 v[80:95], v[6:9], v[120:123], v[80:95]
	v_mfma_f32_32x32x16_bf16 v[96:111], v[10:13], v[124:127], v[96:111]
	v_mfma_f32_32x32x16_bf16 v[80:95], v[142:145], v[124:127], v[80:95]
	s_cbranch_vccnz .LBB0_3644
	v_or_b32_e32 v2, s4, v129
	v_sub_u32_e32 v2, v134, v2
	v_subrev_u32_e32 v3, 32, v2
	v_cmp_gt_u32_e64 s[4:5], s1, v3
	v_add_u32_e32 v3, -1, v2
	v_cmp_gt_u32_e32 vcc, s1, v2
	s_nop 4
	v_cndmask_b32_e64 v80, v240, v80, s[4:5]
	v_cmp_gt_u32_e64 s[4:5], s1, v3
	v_subrev_u32_e32 v3, 33, v2
	v_cmp_gt_u32_e64 s[6:7], s1, v3
	v_add_u32_e32 v3, -2, v2
	s_brev_b32 s36, -16
	v_cndmask_b32_e64 v81, v240, v81, s[6:7]
	v_cmp_gt_u32_e64 s[6:7], s1, v3
	v_subrev_u32_e32 v3, 34, v2
	v_cmp_gt_u32_e64 s[8:9], s1, v3
	v_add_u32_e32 v3, -3, v2
	s_nop 0
	v_cndmask_b32_e64 v82, v240, v82, s[8:9]
	v_cmp_gt_u32_e64 s[8:9], s1, v3
	v_subrev_u32_e32 v3, 35, v2
	v_cmp_gt_u32_e64 s[10:11], s1, v3
	v_add_u32_e32 v3, -8, v2
	s_nop 0
	v_cndmask_b32_e64 v83, v240, v83, s[10:11]
	v_cmp_gt_u32_e64 s[10:11], s1, v3
	v_subrev_u32_e32 v3, 40, v2
	v_cmp_gt_u32_e64 s[12:13], s1, v3
	v_add_u32_e32 v3, -9, v2
	s_nop 0
	v_cndmask_b32_e64 v84, v240, v84, s[12:13]
	v_cmp_gt_u32_e64 s[12:13], s1, v3
	v_subrev_u32_e32 v3, 41, v2
	v_cmp_gt_u32_e64 s[14:15], s1, v3
	v_add_u32_e32 v3, -10, v2
	s_nop 0
	v_cndmask_b32_e64 v85, v240, v85, s[14:15]
	v_cmp_gt_u32_e64 s[14:15], s1, v3
	v_subrev_u32_e32 v3, 42, v2
	v_cmp_gt_u32_e64 s[16:17], s1, v3
	v_add_u32_e32 v3, -11, v2
	s_nop 0
	v_cndmask_b32_e64 v86, v240, v86, s[16:17]
	v_cmp_gt_u32_e64 s[16:17], s1, v3
	v_subrev_u32_e32 v3, 43, v2
	v_cmp_gt_u32_e64 s[18:19], s1, v3
	v_add_u32_e32 v3, -16, v2
	s_nop 0
	v_cndmask_b32_e64 v87, v240, v87, s[18:19]
	v_cmp_gt_u32_e64 s[18:19], s1, v3
	v_subrev_u32_e32 v3, 48, v2
	v_cmp_gt_u32_e64 s[20:21], s1, v3
	v_subrev_u32_e32 v3, 17, v2
	s_nop 0
	v_cndmask_b32_e64 v88, v240, v88, s[20:21]
	v_cmp_gt_u32_e64 s[20:21], s1, v3
	v_subrev_u32_e32 v3, 49, v2
	v_cmp_gt_u32_e64 s[22:23], s1, v3
	v_subrev_u32_e32 v3, 18, v2
	s_nop 0
	v_cndmask_b32_e64 v89, v240, v89, s[22:23]
	v_cmp_gt_u32_e64 s[22:23], s1, v3
	v_subrev_u32_e32 v3, 50, v2
	v_cmp_gt_u32_e64 s[24:25], s1, v3
	v_subrev_u32_e32 v3, 19, v2
	s_nop 0
	v_cndmask_b32_e64 v90, v240, v90, s[24:25]
	v_cmp_gt_u32_e64 s[24:25], s1, v3
	v_subrev_u32_e32 v3, 51, v2
	v_cmp_gt_u32_e64 s[26:27], s1, v3
	v_subrev_u32_e32 v3, 24, v2
	s_nop 0
	v_cndmask_b32_e64 v91, v240, v91, s[26:27]
	v_cmp_gt_u32_e64 s[26:27], s1, v3
	v_subrev_u32_e32 v3, 56, v2
	v_cmp_gt_u32_e64 s[28:29], s1, v3
	v_subrev_u32_e32 v3, 25, v2
	s_nop 0
	v_cndmask_b32_e64 v92, v240, v92, s[28:29]
	v_cmp_gt_u32_e64 s[28:29], s1, v3
	v_subrev_u32_e32 v3, 57, v2
	v_cmp_gt_u32_e64 s[30:31], s1, v3
	v_subrev_u32_e32 v3, 26, v2
	s_nop 0
	v_cndmask_b32_e64 v93, v240, v93, s[30:31]
	v_cmp_gt_u32_e64 s[30:31], s1, v3
	v_subrev_u32_e32 v3, 58, v2
	v_cmp_gt_u32_e64 s[34:35], s1, v3
	v_subrev_u32_e32 v3, 27, v2
	v_subrev_u32_e32 v2, 59, v2
	v_cndmask_b32_e64 v94, v240, v94, s[34:35]
	v_cmp_gt_u32_e64 s[34:35], s1, v3
	v_cmp_lt_u32_e64 s[36:37], s36, v2
	s_and_saveexec_b64 s[46:47], s[36:37]
	v_mov_b32_e32 v95, s61
	s_or_b64 exec, exec, s[46:47]
	v_cndmask_b32_e32 v96, v240, v96, vcc
	v_cndmask_b32_e64 v97, v240, v97, s[4:5]
	v_cndmask_b32_e64 v98, v240, v98, s[6:7]
	v_cndmask_b32_e64 v99, v240, v99, s[8:9]
	v_cndmask_b32_e64 v100, v240, v100, s[10:11]
	v_cndmask_b32_e64 v101, v240, v101, s[12:13]
	v_cndmask_b32_e64 v102, v240, v102, s[14:15]
	v_cndmask_b32_e64 v103, v240, v103, s[16:17]
	v_cndmask_b32_e64 v104, v240, v104, s[18:19]
	v_cndmask_b32_e64 v105, v240, v105, s[20:21]
	v_cndmask_b32_e64 v106, v240, v106, s[22:23]
	v_cndmask_b32_e64 v107, v240, v107, s[24:25]
	v_cndmask_b32_e64 v108, v240, v108, s[26:27]
	v_cndmask_b32_e64 v109, v240, v109, s[28:29]
	v_cndmask_b32_e64 v110, v240, v110, s[30:31]
	v_cndmask_b32_e64 v111, v240, v111, s[34:35]

.LBB0_3733:
	s_waitcnt vmcnt(0)
	s_lshl_b32 s98, s0, 15
	s_cmp_lg_u32 s84, 0
	s_waitcnt lgkmcnt(0)
	s_barrier
	v_add3_u32 v111, s98, v162, v163
	ds_read_b128 v[66:69], v111
	ds_read_b128 v[70:73], v111 offset:512
	ds_read_b128 v[106:109], v111 offset:2048
	ds_read_b128 v[164:167], v111 offset:2560
	s_cbranch_scc0 .LBB0_3748
	s_lshl_b32 s9, s0, 15
	s_ff1_i32_b32 s85, s84
	s_xor_b32 s6, s9, 0x8000
	s_add_i32 s6, s6, 0
	s_lshl_b32 s92, s85, 15
	v_lshl_add_u64 v[214:215], v[104:105], 0, s[92:93]
	s_add_i32 s7, s6, s4
	v_lshl_add_u64 v[216:217], s[74:75], 1, v[214:215]
	s_add_i32 s6, s6, s5
	s_mov_b32 m0, s7
	v_lshl_add_u64 v[214:215], s[94:95], 1, v[214:215]
	global_load_lds_dwordx4 v[216:217], off
	s_mov_b32 m0, s6
	s_nop 0
	global_load_lds_dwordx4 v[214:215], off
	v_lshl_add_u64 v[214:215], v[102:103], 0, s[92:93]
	v_lshl_add_u64 v[216:217], s[70:71], 1, v[214:215]
	s_add_i32 m0, s7, 0x4000
	v_lshl_add_u64 v[214:215], s[66:67], 1, v[214:215]
	global_load_lds_dwordx4 v[216:217], off
	s_add_i32 m0, s6, 0x4000
	s_add_i32 s6, s84, -1
	global_load_lds_dwordx4 v[214:215], off
	s_and_b32 s84, s6, s84
	s_cbranch_execnz .LBB0_3736

.LBB0_3736:
	s_add_i32 s92, s9, 0
	s_lshl_b32 s10, s8, 6
	v_readfirstlane_b32 s9, v156
	s_waitcnt lgkmcnt(0)
	v_mfma_f32_32x32x16_bf16 v[82:97], v[66:69], v[112:115], 0
	v_mfma_f32_32x32x16_bf16 v[66:81], v[70:73], v[112:115], 0
	ds_read_b128 v[168:171], v111 offset:4096
	ds_read_b128 v[172:175], v111 offset:4608
	v_mfma_f32_32x32x16_bf16 v[82:97], v[106:109], v[116:119], v[82:97]
	v_mfma_f32_32x32x16_bf16 v[66:81], v[164:167], v[116:119], v[66:81]
	ds_read_b128 v[106:109], v111 offset:6144
	ds_read_b128 v[164:167], v111 offset:6656
	s_waitcnt lgkmcnt(0)
	v_mfma_f32_32x32x16_bf16 v[82:97], v[168:171], v[120:123], v[82:97]
	v_mfma_f32_32x32x16_bf16 v[66:81], v[172:175], v[120:123], v[66:81]
	ds_read_b128 v[168:171], v111 offset:8192
	ds_read_b128 v[172:175], v111 offset:8704
	v_mfma_f32_32x32x16_bf16 v[82:97], v[106:109], v[124:127], v[82:97]
	v_mfma_f32_32x32x16_bf16 v[66:81], v[164:167], v[124:127], v[66:81]
	ds_read_b128 v[106:109], v111 offset:10240
	ds_read_b128 v[164:167], v111 offset:10752
	s_waitcnt lgkmcnt(0)
	v_mfma_f32_32x32x16_bf16 v[82:97], v[168:171], v[128:131], v[82:97]
	v_mfma_f32_32x32x16_bf16 v[66:81], v[172:175], v[128:131], v[66:81]
	ds_read_b128 v[168:171], v111 offset:12288
	ds_read_b128 v[172:175], v111 offset:12800
	v_mfma_f32_32x32x16_bf16 v[82:97], v[106:109], v[132:135], v[82:97]
	v_mfma_f32_32x32x16_bf16 v[66:81], v[164:167], v[132:135], v[66:81]
	ds_read_b128 v[106:109], v111 offset:14336
	ds_read_b128 v[164:167], v111 offset:14848
	s_waitcnt lgkmcnt(0)
	v_mfma_f32_32x32x16_bf16 v[82:97], v[168:171], v[136:139], v[82:97]
	v_mfma_f32_32x32x16_bf16 v[66:81], v[172:175], v[136:139], v[66:81]
	v_mfma_f32_32x32x16_bf16 v[82:97], v[106:109], v[140:143], v[82:97]
	v_lshrrev_b32_e32 v106, s8, v110
	s_or_b32 s8, s10, 63
	s_cmp_gt_i32 s8, s9
	v_and_b32_e32 v106, 1, v106
	s_cselect_b64 s[8:9], -1, 0
	v_cmp_eq_u32_e64 s[6:7], 1, v106
	s_and_b64 vcc, exec, s[8:9]
	v_mfma_f32_32x32x16_bf16 v[66:81], v[164:167], v[140:143], v[66:81]
	s_cbranch_vccnz .LBB0_3738
	v_cndmask_b32_e64 v106, 0, 1, s[6:7]
	v_cmp_ne_u32_e32 vcc, 0, v106
	s_cmp_lg_u64 vcc, exec
	s_cselect_b64 s[8:9], -1, 0

.LBB0_3758:
	s_waitcnt vmcnt(0)
	s_lshl_b32 s98, s2, 15
	s_cmp_lg_u32 s0, 0
	s_waitcnt lgkmcnt(0)
	s_barrier
	v_add3_u32 v0, s98, v162, v163
	ds_read_b128 v[2:5], v0
	ds_read_b128 v[6:9], v0 offset:512
	ds_read_b128 v[10:13], v0 offset:2048
	ds_read_b128 v[166:169], v0 offset:2560
	s_cbranch_scc0 .LBB0_3771
	s_lshl_b32 s8, s2, 15
	s_ff1_i32_b32 s3, s0
	s_xor_b32 s6, s8, 0x8000
	s_add_i32 s6, s6, 0
	s_lshl_b32 s92, s3, 15
	v_lshl_add_u64 v[214:215], v[150:151], 0, s[92:93]
	s_add_i32 s7, s6, s4
	v_lshl_add_u64 v[216:217], s[74:75], 1, v[214:215]
	s_add_i32 s6, s6, s5
	s_mov_b32 m0, s7
	v_lshl_add_u64 v[214:215], s[94:95], 1, v[214:215]
	global_load_lds_dwordx4 v[216:217], off
	s_mov_b32 m0, s6
	s_nop 0
	global_load_lds_dwordx4 v[214:215], off
	v_lshl_add_u64 v[214:215], v[144:145], 0, s[92:93]
	v_lshl_add_u64 v[216:217], s[70:71], 1, v[214:215]
	s_add_i32 m0, s7, 0x4000
	v_lshl_add_u64 v[214:215], s[66:67], 1, v[214:215]
	global_load_lds_dwordx4 v[216:217], off
	s_add_i32 m0, s6, 0x4000
	s_add_i32 s6, s0, -1
	global_load_lds_dwordx4 v[214:215], off
	s_and_b32 s0, s6, s0
	s_cbranch_execnz .LBB0_3761

.LBB0_3761:
	s_add_i32 s42, s8, 0
	s_lshl_b32 s6, s9, 6
	v_readfirstlane_b32 s7, v156
	s_or_b32 s8, s6, 63
	s_cmp_le_i32 s8, s7
	s_cselect_b64 s[8:9], -1, 0
	s_waitcnt lgkmcnt(0)
	v_mfma_f32_32x32x16_bf16 v[96:111], v[2:5], v[112:115], 0
	s_addk_i32 s7, 0xfe1f
	s_cmp_gt_i32 s6, s7
	s_cselect_b64 s[10:11], -1, 0
	s_and_b64 s[8:9], s[8:9], s[10:11]
	s_and_b64 vcc, exec, s[8:9]
	v_mfma_f32_32x32x16_bf16 v[80:95], v[6:9], v[112:115], 0
	ds_read_b128 v[2:5], v0 offset:4096
	ds_read_b128 v[6:9], v0 offset:4608
	v_mfma_f32_32x32x16_bf16 v[96:111], v[10:13], v[116:119], v[96:111]
	v_mfma_f32_32x32x16_bf16 v[80:95], v[166:169], v[116:119], v[80:95]
	ds_read_b128 v[10:13], v0 offset:6144
	ds_read_b128 v[166:169], v0 offset:6656
	s_waitcnt lgkmcnt(0)
	v_mfma_f32_32x32x16_bf16 v[96:111], v[2:5], v[120:123], v[96:111]
	v_mfma_f32_32x32x16_bf16 v[80:95], v[6:9], v[120:123], v[80:95]
	ds_read_b128 v[2:5], v0 offset:8192
	ds_read_b128 v[6:9], v0 offset:8704
	v_mfma_f32_32x32x16_bf16 v[96:111], v[10:13], v[124:127], v[96:111]
	v_mfma_f32_32x32x16_bf16 v[80:95], v[166:169], v[124:127], v[80:95]
	ds_read_b128 v[10:13], v0 offset:10240
	ds_read_b128 v[166:169], v0 offset:10752
	s_waitcnt lgkmcnt(0)
	v_mfma_f32_32x32x16_bf16 v[96:111], v[2:5], v[128:131], v[96:111]
	v_mfma_f32_32x32x16_bf16 v[80:95], v[6:9], v[128:131], v[80:95]
	ds_read_b128 v[2:5], v0 offset:12288
	ds_read_b128 v[6:9], v0 offset:12800
	v_mfma_f32_32x32x16_bf16 v[96:111], v[10:13], v[132:135], v[96:111]
	v_mfma_f32_32x32x16_bf16 v[80:95], v[166:169], v[132:135], v[80:95]
	ds_read_b128 v[10:13], v0 offset:14336
	ds_read_b128 v[166:169], v0 offset:14848
	s_waitcnt lgkmcnt(0)
	v_mfma_f32_32x32x16_bf16 v[96:111], v[2:5], v[136:139], v[96:111]
	v_mfma_f32_32x32x16_bf16 v[80:95], v[6:9], v[136:139], v[80:95]
	v_mfma_f32_32x32x16_bf16 v[96:111], v[10:13], v[140:143], v[96:111]
	v_mfma_f32_32x32x16_bf16 v[80:95], v[166:169], v[140:143], v[80:95]
	s_cbranch_vccnz .LBB0_3765
	v_or_b32_e32 v0, s6, v161
	v_sub_u32_e32 v0, v156, v0
	v_subrev_u32_e32 v2, 32, v0
	v_cmp_gt_u32_e64 s[6:7], s89, v2
	v_add_u32_e32 v2, -1, v0
	v_cmp_gt_u32_e32 vcc, s89, v0
	s_nop 4
	v_cndmask_b32_e64 v80, v240, v80, s[6:7]
	v_cmp_gt_u32_e64 s[6:7], s89, v2
	v_subrev_u32_e32 v2, 33, v0
	v_cmp_gt_u32_e64 s[8:9], s89, v2
	v_add_u32_e32 v2, -2, v0
	s_movk_i32 s38, 0x1ff
	v_cndmask_b32_e64 v81, v240, v81, s[8:9]
	v_cmp_gt_u32_e64 s[8:9], s89, v2
	v_subrev_u32_e32 v2, 34, v0
	v_cmp_gt_u32_e64 s[10:11], s89, v2
	v_add_u32_e32 v2, -3, v0
	s_nop 0
	v_cndmask_b32_e64 v82, v240, v82, s[10:11]
	v_cmp_gt_u32_e64 s[10:11], s89, v2
	v_subrev_u32_e32 v2, 35, v0
	v_cmp_gt_u32_e64 s[12:13], s89, v2
	v_add_u32_e32 v2, -8, v0
	s_nop 0
	v_cndmask_b32_e64 v83, v240, v83, s[12:13]
	v_cmp_gt_u32_e64 s[12:13], s89, v2
	v_subrev_u32_e32 v2, 40, v0
	v_cmp_gt_u32_e64 s[14:15], s89, v2
	v_add_u32_e32 v2, -9, v0
	s_nop 0
	v_cndmask_b32_e64 v84, v240, v84, s[14:15]
	v_cmp_gt_u32_e64 s[14:15], s89, v2
	v_subrev_u32_e32 v2, 41, v0
	v_cmp_gt_u32_e64 s[16:17], s89, v2
	v_add_u32_e32 v2, -10, v0
	s_nop 0
	v_cndmask_b32_e64 v85, v240, v85, s[16:17]
	v_cmp_gt_u32_e64 s[16:17], s89, v2
	v_subrev_u32_e32 v2, 42, v0
	v_cmp_gt_u32_e64 s[18:19], s89, v2
	v_add_u32_e32 v2, -11, v0
	s_nop 0
	v_cndmask_b32_e64 v86, v240, v86, s[18:19]
	v_cmp_gt_u32_e64 s[18:19], s89, v2
	v_subrev_u32_e32 v2, 43, v0
	v_cmp_gt_u32_e64 s[20:21], s89, v2
	v_add_u32_e32 v2, -16, v0
	s_nop 0
	v_cndmask_b32_e64 v87, v240, v87, s[20:21]
	v_cmp_gt_u32_e64 s[20:21], s89, v2
	v_subrev_u32_e32 v2, 48, v0
	v_cmp_gt_u32_e64 s[22:23], s89, v2
	v_subrev_u32_e32 v2, 17, v0
	s_nop 0
	v_cndmask_b32_e64 v88, v240, v88, s[22:23]
	v_cmp_gt_u32_e64 s[22:23], s89, v2
	v_subrev_u32_e32 v2, 49, v0
	v_cmp_gt_u32_e64 s[24:25], s89, v2
	v_subrev_u32_e32 v2, 18, v0
	s_nop 0
	v_cndmask_b32_e64 v89, v240, v89, s[24:25]
	v_cmp_gt_u32_e64 s[24:25], s89, v2
	v_subrev_u32_e32 v2, 50, v0
	v_cmp_gt_u32_e64 s[26:27], s89, v2
	v_subrev_u32_e32 v2, 19, v0
	s_nop 0
	v_cndmask_b32_e64 v90, v240, v90, s[26:27]
	v_cmp_gt_u32_e64 s[26:27], s89, v2
	v_subrev_u32_e32 v2, 51, v0
	v_cmp_gt_u32_e64 s[28:29], s89, v2
	v_subrev_u32_e32 v2, 24, v0
	s_nop 0
	v_cndmask_b32_e64 v91, v240, v91, s[28:29]
	v_cmp_gt_u32_e64 s[28:29], s89, v2
	v_subrev_u32_e32 v2, 56, v0
	v_cmp_gt_u32_e64 s[30:31], s89, v2
	v_subrev_u32_e32 v2, 25, v0
	s_nop 0
	v_cndmask_b32_e64 v92, v240, v92, s[30:31]
	v_cmp_gt_u32_e64 s[30:31], s89, v2
	v_subrev_u32_e32 v2, 57, v0
	v_cmp_gt_u32_e64 s[34:35], s89, v2
	v_subrev_u32_e32 v2, 26, v0
	s_nop 0
	v_cndmask_b32_e64 v93, v240, v93, s[34:35]
	v_cmp_gt_u32_e64 s[34:35], s89, v2
	v_subrev_u32_e32 v2, 58, v0
	v_cmp_gt_u32_e64 s[36:37], s89, v2
	v_subrev_u32_e32 v2, 27, v0
	v_subrev_u32_e32 v0, 59, v0
	v_cndmask_b32_e64 v94, v240, v94, s[36:37]
	v_cmp_gt_u32_e64 s[36:37], s89, v2
	v_cmp_lt_u32_e64 s[38:39], s38, v0
	s_and_saveexec_b64 s[40:41], s[38:39]
	v_mov_b32_e32 v95, s61
	s_or_b64 exec, exec, s[40:41]
	v_cndmask_b32_e32 v96, v240, v96, vcc
	v_cndmask_b32_e64 v97, v240, v97, s[6:7]
	v_cndmask_b32_e64 v98, v240, v98, s[8:9]
	v_cndmask_b32_e64 v99, v240, v99, s[10:11]
	v_cndmask_b32_e64 v100, v240, v100, s[12:13]
	v_cndmask_b32_e64 v101, v240, v101, s[14:15]
	v_cndmask_b32_e64 v102, v240, v102, s[16:17]
	v_cndmask_b32_e64 v103, v240, v103, s[18:19]
	v_cndmask_b32_e64 v104, v240, v104, s[20:21]
	v_cndmask_b32_e64 v105, v240, v105, s[22:23]
	v_cndmask_b32_e64 v106, v240, v106, s[24:25]
	v_cndmask_b32_e64 v107, v240, v107, s[26:27]
	v_cndmask_b32_e64 v108, v240, v108, s[28:29]
	v_cndmask_b32_e64 v109, v240, v109, s[30:31]
	v_cndmask_b32_e64 v110, v240, v110, s[34:35]
	v_cndmask_b32_e64 v111, v240, v111, s[36:37]
